# MoE combine loop: the 8 gate-table loads of a token pair issued before the next pair's 12 row loads (free VGPRs); first-use wait counted so the row prefetch stays in flight; 2 of the 4 per-group full
# speedup vs baseline: 1.0058x; 1.0058x over previous
; DEV float bflo(unsigned u) { return __uint_as_float(u << 16); }
; DEV float bfhi(unsigned u) { return __uint_as_float(u & 0xffff0000u); }
; DEV void phase_combine(const Params& p, int layer, LAS char* lds, bool have_tables = false) {
;     ...
;     for (int tok0 = t0; tok0 < ntok; tok0 += step) {
;         const int tn = tok0 + step, tnn = tn + step;
;         u32x4 tif[2] = {tin[0], tin[1]};
;         if (tnn < ntok) { tif[0] = TIE[tnn]; tif[1] = TIE[tnn + 1]; }
;         if (tn < ntok) { issue_rows(tn, tin[0], nxt[0]); issue_rows(tn + 1, tin[1], nxt[1]); }
; #pragma unroll
;         for (int q = 0; q < 2; ++q) { const int tok = tok0 + q;
;             float xv[2][8];
; #pragma unroll
;             for (int j = 0; j < 2; ++j)
; #pragma unroll
;                 for (int e = 0; e < 4; ++e) { xv[j][2 * e] = bflo(cur[q].xr[j][e]); xv[j][2 * e + 1] = bfhi(cur[q].xr[j][e]); }
;             bf16_t* X = (bf16_t*)(ws + WS_X) + (size_t)tok * 1024;
;             const float* g2 = mod + mod_row(tok) * 6144 + 5120;
;             const float w1 = cur[q].w1, w2 = cur[q].w2;
; #pragma unroll
;             for (int j = 0; j < 2; ++j) { const int col = 8 * lane + 512 * j;
;                 const f32x4 ga = *(const f32x4*)(g2 + col), gb = *(const f32x4*)(g2 + col + 4);
; #pragma unroll
;                 for (int e = 0; e < 4; ++e) { const float gg0 = e < 2 ? ga[2 * e] : gb[2 * e - 4], gg1 = e < 2 ? ga[2 * e + 1] : gb[2 * e - 3];
;                     xv[j][2 * e] += gg0 * (w1 * bflo(cur[q].ya[j][e]) + w2 * bflo(cur[q].yb[j][e])); xv[j][2 * e + 1] += gg1 * (w1 * bfhi(cur[q].ya[j][e]) + w2 * bfhi(cur[q].yb[j][e])); }
.LBB0_1491:
	s_or_b64 exec, exec, s[6:7]
	v_add_u32_e32 v182, -1, v142
	v_min_i32_e32 v182, 0x8000, v182
	v_ashrrev_i32_e32 v182, 14, v182
	v_mul_i32_i24_e32 v182, 0x1800, v182
	v_ashrrev_i32_e32 v183, 31, v182
	v_lshl_add_u64 v[182:183], v[182:183], 2, s[46:47]
	s_mov_b64 s[2:3], 0x15000
	v_lshl_add_u64 v[182:183], v[182:183], 0, s[2:3]
	v_lshl_add_u64 v[184:185], v[182:183], 0, v[178:179]
	global_load_dwordx4 v[166:169], v[184:185], off
	global_load_dwordx4 v[170:173], v[184:185], off offset:16
	v_lshlrev_b32_e32 v188, 2, v116
	v_mov_b32_e32 v189, v179
	v_lshl_add_u64 v[184:185], v[182:183], 0, v[188:189]
	global_load_dwordx4 v[174:177], v[184:185], off
	global_load_dwordx4 v[198:201], v[184:185], off offset:16
	v_min_i32_e32 v182, 0x8000, v142
	v_ashrrev_i32_e32 v182, 14, v182
	v_mul_i32_i24_e32 v182, 0x1800, v182
	v_ashrrev_i32_e32 v183, 31, v182
	v_lshl_add_u64 v[182:183], v[182:183], 2, s[46:47]
	v_lshl_add_u64 v[182:183], v[182:183], 0, s[2:3]
	v_lshl_add_u64 v[184:185], v[182:183], 0, v[178:179]
	global_load_dwordx4 v[202:205], v[184:185], off
	global_load_dwordx4 v[210:213], v[184:185], off offset:16
	v_lshl_add_u64 v[184:185], v[182:183], 0, v[188:189]
	global_load_dwordx4 v[214:217], v[184:185], off
	global_load_dwordx4 v[228:231], v[184:185], off offset:16
	v_readlane_b32 s2, v254, 32
	v_readlane_b32 s3, v254, 33
	s_nop 0
	v_add_u32_e32 v134, s2, v142
	v_add_u32_e32 v138, -1, v134
	v_cmp_gt_i32_e32 vcc, s12, v138
	v_cmp_le_i32_e64 s[38:39], s12, v138
	s_and_saveexec_b64 s[6:7], vcc
	s_cselect_b32 s100, 1, 0
	s_cbranch_execz .LBB0_1493
	v_bfe_u32 v6, v96, 16, 16
	v_readlane_b32 s2, v253, 58
	v_bfe_u32 v7, v97, 16, 16
	v_and_b32_e32 v8, 0xffff, v96
	v_lshl_add_u32 v6, v6, 2, s2
	ds_read_b32 v6, v6
	v_lshl_add_u32 v7, v7, 2, s2
	ds_read_b32 v7, v7
	v_ashrrev_i32_e32 v139, 31, v138
	v_lshlrev_b64 v[10:11], 11, v[138:139]
	s_waitcnt lgkmcnt(1)
	v_lshl_add_u32 v6, v6, 8, v8
	v_and_b32_e32 v8, 0xffff, v97
	s_waitcnt lgkmcnt(0)
	v_lshl_add_u32 v8, v7, 8, v8
	v_ashrrev_i32_e32 v7, 31, v6
	v_lshlrev_b64 v[6:7], 11, v[6:7]
	v_ashrrev_i32_e32 v9, 31, v8
	v_bfe_u32 v22, v112, 16, 16
	v_lshlrev_b64 v[8:9], 11, v[8:9]
	v_lshl_add_u64 v[10:11], v[122:123], 0, v[10:11]
	v_lshl_add_u64 v[18:19], v[124:125], 0, v[6:7]
	v_lshl_add_u32 v22, v22, 2, s2
	v_bfe_u32 v23, v113, 16, 16
	v_lshl_add_u64 v[26:27], v[124:125], 0, v[8:9]
	global_load_dwordx4 v[6:9], v[10:11], off
	s_nop 0
	global_load_dwordx4 v[10:13], v[10:11], off offset:1024
	s_nop 0
	global_load_dwordx4 v[14:17], v[18:19], off
	s_nop 0
	global_load_dwordx4 v[18:21], v[18:19], off offset:1024
	v_lshl_add_u32 v23, v23, 2, s2
	ds_read_b32 v30, v22
	ds_read_b32 v31, v23
	v_and_b32_e32 v32, 0xffff, v112
	v_ashrrev_i32_e32 v135, 31, v134
	v_lshlrev_b64 v[34:35], 11, v[134:135]
	s_waitcnt lgkmcnt(1)
	v_lshl_add_u32 v30, v30, 8, v32
	v_and_b32_e32 v32, 0xffff, v113
	s_waitcnt lgkmcnt(0)
	v_lshl_add_u32 v32, v31, 8, v32
	v_ashrrev_i32_e32 v31, 31, v30
	v_ashrrev_i32_e32 v33, 31, v32
	v_lshlrev_b64 v[30:31], 11, v[30:31]
	v_lshlrev_b64 v[32:33], 11, v[32:33]
	v_lshl_add_u64 v[34:35], v[122:123], 0, v[34:35]
	v_lshl_add_u64 v[42:43], v[124:125], 0, v[30:31]
	v_lshl_add_u64 v[44:45], v[124:125], 0, v[32:33]
	global_load_dwordx4 v[22:25], v[26:27], off
	s_nop 0
	global_load_dwordx4 v[26:29], v[26:27], off offset:1024
	s_nop 0
	global_load_dwordx4 v[30:33], v[34:35], off
	s_nop 0
	global_load_dwordx4 v[34:37], v[34:35], off offset:1024
	s_nop 0
	global_load_dwordx4 v[38:41], v[42:43], off
	global_load_dwordx4 v[46:49], v[42:43], off offset:1024
	global_load_dwordx4 v[50:53], v[44:45], off
	s_nop 0
	global_load_dwordx4 v[42:45], v[44:45], off offset:1024
	v_mov_b32_e32 v117, v115
	v_mov_b32_e32 v139, v114
	v_mov_b32_e32 v140, v98
	v_mov_b32_e32 v141, v99
.LBB0_1493:
	s_or_b64 exec, exec, s[6:7]
	v_add_u32_e32 v96, -1, v142
	v_min_i32_e32 v96, 0x8000, v96
	v_ashrrev_i32_e32 v96, 14, v96
	v_mul_i32_i24_e32 v112, 0x1800, v96
	v_ashrrev_i32_e32 v113, 31, v112
	v_lshl_add_u64 v[96:97], v[112:113], 2, s[46:47]
	s_mov_b64 s[2:3], 0x15000
	v_lshl_add_u64 v[114:115], v[96:97], 0, s[2:3]
	v_lshl_add_u64 v[96:97], v[114:115], 0, v[178:179]
	v_lshlrev_b32_e32 v150, 16, v104
	v_and_b32_e32 v151, 0xffff0000, v108
	v_pk_mul_f32 v[150:151], v[82:83], v[150:151] op_sel:[1,0] op_sel_hi:[0,1]
	v_lshlrev_b32_e32 v152, 16, v108
	v_and_b32_e32 v153, 0xffff0000, v104
	v_lshlrev_b32_e32 v148, 16, v100
	v_and_b32_e32 v149, 0xffff0000, v100
	v_pk_fma_f32 v[150:151], v[82:83], v[152:153], v[150:151]
	v_lshlrev_b32_e32 v104, 16, v109
	v_lshlrev_b32_e32 v100, 16, v101
	v_and_b32_e32 v101, 0xffff0000, v101
	v_lshlrev_b32_e32 v108, 16, v110
	v_readlane_b32 s2, v254, 55
	v_readlane_b32 s3, v254, 56
	s_mov_b64 s[6:7], -1
	s_and_b64 vcc, exec, s[2:3]
	s_cmp_eq_u32 s100, 0
	s_cbranch_scc1 .Lcmb_w0
	s_waitcnt vmcnt(12)
	s_branch .Lcmb_wd

; DEV unsigned cvtpk(float lo, float hi) { f32x2 v = {lo, hi}; bf16v2 r = __builtin_convertvector(v, bf16v2); return __builtin_bit_cast(unsigned, r); }
; DEV float bflo(unsigned u) { return __uint_as_float(u << 16); }
; DEV float bfhi(unsigned u) { return __uint_as_float(u & 0xffff0000u); }
; DEV void phase_combine(const Params& p, int layer, LAS char* lds, bool have_tables = false) {
;     ...
;             for (int j = 0; j < 2; ++j) { const int col = 8 * lane + 512 * j;
;                 const f32x4 ga = *(const f32x4*)(g2 + col), gb = *(const f32x4*)(g2 + col + 4);
; #pragma unroll
;                 for (int e = 0; e < 4; ++e) { const float gg0 = e < 2 ? ga[2 * e] : gb[2 * e - 4], gg1 = e < 2 ? ga[2 * e + 1] : gb[2 * e - 3];
;                     xv[j][2 * e] += gg0 * (w1 * bflo(cur[q].ya[j][e]) + w2 * bflo(cur[q].yb[j][e])); xv[j][2 * e + 1] += gg1 * (w1 * bfhi(cur[q].ya[j][e]) + w2 * bfhi(cur[q].yb[j][e])); }
;                 if (layer == 0) *(u32x4*)(X + col) = (u32x4){cvtpk(xv[j][0], xv[j][1]), cvtpk(xv[j][2], xv[j][3]), cvtpk(xv[j][4], xv[j][5]), cvtpk(xv[j][6], xv[j][7])};
.Lcmb_wd:
	v_pk_fma_f32 v[96:97], v[150:151], v[166:167], v[148:149]
	v_lshlrev_b32_e32 v148, 16, v105
	v_and_b32_e32 v149, 0xffff0000, v109
	v_pk_mul_f32 v[148:149], v[82:83], v[148:149] op_sel:[1,0] op_sel_hi:[0,1]
	v_and_b32_e32 v105, 0xffff0000, v105
	v_pk_fma_f32 v[104:105], v[82:83], v[104:105], v[148:149]
	v_and_b32_e32 v109, 0xffff0000, v106
	v_pk_fma_f32 v[98:99], v[104:105], v[168:169], v[100:101]
	v_lshlrev_b32_e32 v104, 16, v106
	v_and_b32_e32 v105, 0xffff0000, v110
	v_pk_mul_f32 v[104:105], v[82:83], v[104:105] op_sel:[1,0] op_sel_hi:[0,1]
	v_lshlrev_b32_e32 v100, 16, v102
	v_and_b32_e32 v101, 0xffff0000, v102
	v_pk_fma_f32 v[104:105], v[82:83], v[108:109], v[104:105]
	v_lshlrev_b32_e32 v106, 16, v111
	v_pk_fma_f32 v[100:101], v[104:105], v[170:171], v[100:101]
	v_lshlrev_b32_e32 v104, 16, v107
	v_and_b32_e32 v105, 0xffff0000, v111
	v_pk_mul_f32 v[104:105], v[82:83], v[104:105] op_sel:[1,0] op_sel_hi:[0,1]
	v_and_b32_e32 v107, 0xffff0000, v107
	v_lshlrev_b32_e32 v102, 16, v103
	v_and_b32_e32 v103, 0xffff0000, v103
	v_pk_fma_f32 v[104:105], v[82:83], v[106:107], v[104:105]
	s_nop 0
	v_pk_fma_f32 v[102:103], v[104:105], v[172:173], v[102:103]
	s_cbranch_vccz .LBB0_1495
	v_add_co_u32_e32 v104, vcc, 0xfffff000, v130
	s_mov_b64 s[6:7], 0
	s_nop 0
	v_addc_co_u32_e32 v105, vcc, -1, v131, vcc
	global_store_dwordx4 v[104:105], v[96:99], off offset:-2064
	global_store_dwordx4 v[104:105], v[100:103], off offset:-2048

; DEV unsigned cvtpk(float lo, float hi) { f32x2 v = {lo, hi}; bf16v2 r = __builtin_convertvector(v, bf16v2); return __builtin_bit_cast(unsigned, r); }
; DEV float bflo(unsigned u) { return __uint_as_float(u << 16); }
; DEV float bfhi(unsigned u) { return __uint_as_float(u & 0xffff0000u); }
; DEV void phase_combine(const Params& p, int layer, LAS char* lds, bool have_tables = false) {
;     ...
;             for (int j = 0; j < 2; ++j) { const int col = 8 * lane + 512 * j;
;                 const f32x4 ga = *(const f32x4*)(g2 + col), gb = *(const f32x4*)(g2 + col + 4);
; #pragma unroll
;                 for (int e = 0; e < 4; ++e) { const float gg0 = e < 2 ? ga[2 * e] : gb[2 * e - 4], gg1 = e < 2 ? ga[2 * e + 1] : gb[2 * e - 3];
;                     xv[j][2 * e] += gg0 * (w1 * bflo(cur[q].ya[j][e]) + w2 * bflo(cur[q].yb[j][e])); xv[j][2 * e + 1] += gg1 * (w1 * bfhi(cur[q].ya[j][e]) + w2 * bfhi(cur[q].yb[j][e])); }
;                 if (layer == 0) *(u32x4*)(X + col) = (u32x4){cvtpk(xv[j][0], xv[j][1]), cvtpk(xv[j][2], xv[j][3]), cvtpk(xv[j][4], xv[j][5]), cvtpk(xv[j][6], xv[j][7])};
.LBB0_1497:
	v_lshlrev_b32_e32 v104, 2, v116
	v_mov_b32_e32 v105, v179
	v_lshlrev_b32_e32 v146, 16, v92
	v_and_b32_e32 v147, 0xffff0000, v92
	v_lshlrev_b32_e32 v148, 16, v93
	v_and_b32_e32 v149, 0xffff0000, v93
	v_lshl_add_u64 v[92:93], v[114:115], 0, v[104:105]
	v_lshlrev_b32_e32 v150, 16, v94
	v_and_b32_e32 v151, 0xffff0000, v94
	v_lshlrev_b32_e32 v152, 16, v95
	v_and_b32_e32 v153, 0xffff0000, v95
	v_pk_mov_b32 v[144:145], v[82:83], v[82:83] op_sel:[1,0]
	v_lshlrev_b32_e32 v114, 16, v84
	v_and_b32_e32 v115, 0xffff0000, v88
	v_pk_mul_f32 v[114:115], v[144:145], v[114:115]
	v_lshlrev_b32_e32 v154, 16, v88
	v_and_b32_e32 v155, 0xffff0000, v84
	v_pk_fma_f32 v[114:115], v[82:83], v[154:155], v[114:115]
	v_lshlrev_b32_e32 v84, 16, v89
	v_lshlrev_b32_e32 v88, 16, v90
	v_readlane_b32 s2, v254, 55
	v_readlane_b32 s3, v254, 56
	s_mov_b64 s[6:7], -1
	s_andn2_b64 vcc, exec, s[2:3]
	v_pk_fma_f32 v[92:93], v[114:115], v[174:175], v[146:147]
	v_lshlrev_b32_e32 v114, 16, v85
	v_and_b32_e32 v115, 0xffff0000, v89
	v_pk_mul_f32 v[114:115], v[144:145], v[114:115]
	v_and_b32_e32 v85, 0xffff0000, v85
	v_pk_fma_f32 v[84:85], v[82:83], v[84:85], v[114:115]
	v_and_b32_e32 v89, 0xffff0000, v86
	v_pk_fma_f32 v[94:95], v[84:85], v[176:177], v[148:149]
	v_lshlrev_b32_e32 v84, 16, v86
	v_and_b32_e32 v85, 0xffff0000, v90
	v_pk_mul_f32 v[84:85], v[144:145], v[84:85]
	v_lshlrev_b32_e32 v86, 16, v91
	v_pk_fma_f32 v[84:85], v[82:83], v[88:89], v[84:85]
	v_lshlrev_b32_e32 v88, 16, v87
	v_and_b32_e32 v89, 0xffff0000, v91
	v_pk_mul_f32 v[88:89], v[144:145], v[88:89]
	v_and_b32_e32 v87, 0xffff0000, v87
	v_pk_fma_f32 v[82:83], v[82:83], v[86:87], v[88:89]
	v_pk_fma_f32 v[84:85], v[84:85], v[198:199], v[150:151]
	v_pk_fma_f32 v[86:87], v[82:83], v[200:201], v[152:153]
	v_cndmask_b32_e64 v82, 0, 1, s[2:3]
	v_cmp_ne_u32_e64 s[40:41], 1, v82
	s_cbranch_vccnz .LBB0_1499
	v_add_co_u32_e32 v82, vcc, 0xfffff000, v130
	s_mov_b64 s[6:7], 0
	s_nop 0
	v_addc_co_u32_e32 v83, vcc, -1, v131, vcc
	global_store_dwordx4 v[82:83], v[92:95], off offset:-16
	global_store_dwordx4 v[130:131], v[84:87], off offset:-4096

; DEV unsigned cvtpk(float lo, float hi) { f32x2 v = {lo, hi}; bf16v2 r = __builtin_convertvector(v, bf16v2); return __builtin_bit_cast(unsigned, r); }
; DEV float bflo(unsigned u) { return __uint_as_float(u << 16); }
; DEV float bfhi(unsigned u) { return __uint_as_float(u & 0xffff0000u); }
; DEV void phase_combine(const Params& p, int layer, LAS char* lds, bool have_tables = false) {
;     ...
;             for (int j = 0; j < 2; ++j) { const int col = 8 * lane + 512 * j;
;                 const f32x4 ga = *(const f32x4*)(g2 + col), gb = *(const f32x4*)(g2 + col + 4);
; #pragma unroll
;                 for (int e = 0; e < 4; ++e) { const float gg0 = e < 2 ? ga[2 * e] : gb[2 * e - 4], gg1 = e < 2 ? ga[2 * e + 1] : gb[2 * e - 3];
;                     xv[j][2 * e] += gg0 * (w1 * bflo(cur[q].ya[j][e]) + w2 * bflo(cur[q].yb[j][e])); xv[j][2 * e + 1] += gg1 * (w1 * bfhi(cur[q].ya[j][e]) + w2 * bfhi(cur[q].yb[j][e])); }
;                 if (layer == 0) *(u32x4*)(X + col) = (u32x4){cvtpk(xv[j][0], xv[j][1]), cvtpk(xv[j][2], xv[j][3]), cvtpk(xv[j][4], xv[j][5]), cvtpk(xv[j][6], xv[j][7])};
.LBB0_1503:
	s_nop 1
	v_min_i32_e32 v82, 0x8000, v142
	v_ashrrev_i32_e32 v82, 14, v82
	v_mul_i32_i24_e32 v86, 0x1800, v82
	v_ashrrev_i32_e32 v87, 31, v86
	v_lshl_add_u64 v[82:83], v[86:87], 2, s[46:47]
	s_mov_b64 s[2:3], 0x15000
	v_lshl_add_u64 v[90:91], v[82:83], 0, s[2:3]
	v_lshl_add_u64 v[82:83], v[90:91], 0, v[178:179]
	v_lshlrev_b32_e32 v100, 16, v78
	v_and_b32_e32 v101, 0xffff0000, v74
	v_lshlrev_b32_e32 v98, 16, v74
	v_and_b32_e32 v99, 0xffff0000, v78
	v_pk_mul_f32 v[100:101], v[136:137], v[100:101] op_sel:[1,0] op_sel_hi:[0,1]
	v_lshlrev_b32_e32 v96, 16, v70
	v_and_b32_e32 v97, 0xffff0000, v70
	v_pk_fma_f32 v[98:99], v[136:137], v[98:99], v[100:101]
	v_lshlrev_b32_e32 v74, 16, v79
	v_lshlrev_b32_e32 v70, 16, v71
	v_and_b32_e32 v71, 0xffff0000, v71
	v_lshlrev_b32_e32 v78, 16, v80
	s_mov_b64 s[6:7], -1
	s_and_b64 vcc, exec, s[40:41]
	v_pk_fma_f32 v[82:83], v[98:99], v[202:203], v[96:97]
	v_lshlrev_b32_e32 v96, 16, v75
	v_and_b32_e32 v75, 0xffff0000, v75
	v_and_b32_e32 v97, 0xffff0000, v79
	v_pk_mul_f32 v[74:75], v[136:137], v[74:75] op_sel:[1,0] op_sel_hi:[0,1]
	v_pk_fma_f32 v[74:75], v[136:137], v[96:97], v[74:75]
	v_and_b32_e32 v79, 0xffff0000, v76
	v_pk_fma_f32 v[84:85], v[74:75], v[204:205], v[70:71]
	v_lshlrev_b32_e32 v74, 16, v76
	v_and_b32_e32 v75, 0xffff0000, v80
	v_pk_mul_f32 v[78:79], v[136:137], v[78:79] op_sel:[1,0] op_sel_hi:[0,1]
	v_lshlrev_b32_e32 v70, 16, v72
	v_and_b32_e32 v71, 0xffff0000, v72
	v_pk_fma_f32 v[74:75], v[136:137], v[74:75], v[78:79]
	v_lshlrev_b32_e32 v76, 16, v81
	v_pk_fma_f32 v[70:71], v[74:75], v[210:211], v[70:71]
	v_lshlrev_b32_e32 v74, 16, v77
	v_and_b32_e32 v77, 0xffff0000, v77
	v_and_b32_e32 v75, 0xffff0000, v81
	v_pk_mul_f32 v[76:77], v[136:137], v[76:77] op_sel:[1,0] op_sel_hi:[0,1]
	v_lshlrev_b32_e32 v72, 16, v73
	v_and_b32_e32 v73, 0xffff0000, v73
	v_pk_fma_f32 v[74:75], v[136:137], v[74:75], v[76:77]
	s_nop 0
	v_pk_fma_f32 v[72:73], v[74:75], v[212:213], v[72:73]
	s_cbranch_vccnz .LBB0_1505
	s_mov_b64 s[6:7], 0
	global_store_dwordx4 v[130:131], v[82:85], off offset:-2064
	global_store_dwordx4 v[130:131], v[70:73], off offset:-2048

; DEV unsigned cvtpk(float lo, float hi) { f32x2 v = {lo, hi}; bf16v2 r = __builtin_convertvector(v, bf16v2); return __builtin_bit_cast(unsigned, r); }
; DEV float bflo(unsigned u) { return __uint_as_float(u << 16); }
; DEV float bfhi(unsigned u) { return __uint_as_float(u & 0xffff0000u); }
; DEV void phase_combine(const Params& p, int layer, LAS char* lds, bool have_tables = false) {
;     ...
;             for (int j = 0; j < 2; ++j) { const int col = 8 * lane + 512 * j;
;                 const f32x4 ga = *(const f32x4*)(g2 + col), gb = *(const f32x4*)(g2 + col + 4);
; #pragma unroll
;                 for (int e = 0; e < 4; ++e) { const float gg0 = e < 2 ? ga[2 * e] : gb[2 * e - 4], gg1 = e < 2 ? ga[2 * e + 1] : gb[2 * e - 3];
;                     xv[j][2 * e] += gg0 * (w1 * bflo(cur[q].ya[j][e]) + w2 * bflo(cur[q].yb[j][e])); xv[j][2 * e + 1] += gg1 * (w1 * bfhi(cur[q].ya[j][e]) + w2 * bfhi(cur[q].yb[j][e])); }
;                 if (layer == 0) *(u32x4*)(X + col) = (u32x4){cvtpk(xv[j][0], xv[j][1]), cvtpk(xv[j][2], xv[j][3]), cvtpk(xv[j][4], xv[j][5]), cvtpk(xv[j][6], xv[j][7])};
.LBB0_1507:
	v_mov_b32_e32 v105, v179
	v_lshl_add_u64 v[78:79], v[90:91], 0, v[104:105]
	v_pk_mov_b32 v[90:91], v[136:137], v[136:137] op_sel:[1,0]
	v_lshlrev_b32_e32 v96, 16, v62
	v_and_b32_e32 v97, 0xffff0000, v66
	v_lshlrev_b32_e32 v98, 16, v66
	v_and_b32_e32 v99, 0xffff0000, v62
	v_lshlrev_b32_e32 v100, 16, v63
	v_lshlrev_b32_e32 v62, 16, v67
	v_and_b32_e32 v63, 0xffff0000, v63
	v_lshlrev_b32_e32 v66, 16, v64
	v_lshlrev_b32_e32 v102, 16, v68
	v_and_b32_e32 v103, 0xffff0000, v64
	v_lshlrev_b32_e32 v108, 16, v65
	v_lshlrev_b32_e32 v64, 16, v69
	v_and_b32_e32 v65, 0xffff0000, v65
	v_and_b32_e32 v101, 0xffff0000, v67
	v_and_b32_e32 v67, 0xffff0000, v68
	v_and_b32_e32 v109, 0xffff0000, v69
	v_pk_mul_f32 v[68:69], v[90:91], v[98:99]
	v_pk_mul_f32 v[62:63], v[90:91], v[62:63]
	v_pk_mul_f32 v[98:99], v[90:91], v[102:103]
	v_pk_mul_f32 v[64:65], v[90:91], v[64:65]
	v_lshlrev_b32_e32 v92, 16, v58
	v_and_b32_e32 v93, 0xffff0000, v58
	v_lshlrev_b32_e32 v58, 16, v59
	v_and_b32_e32 v59, 0xffff0000, v59
	v_lshlrev_b32_e32 v94, 16, v60
	v_and_b32_e32 v95, 0xffff0000, v60
	v_lshlrev_b32_e32 v60, 16, v61
	v_and_b32_e32 v61, 0xffff0000, v61
	v_pk_fma_f32 v[68:69], v[136:137], v[96:97], v[68:69]
	v_pk_fma_f32 v[90:91], v[136:137], v[100:101], v[62:63]
	v_pk_fma_f32 v[66:67], v[136:137], v[66:67], v[98:99]
	v_pk_fma_f32 v[96:97], v[136:137], v[108:109], v[64:65]
	s_and_b64 vcc, exec, s[40:41]
	s_mov_b64 s[6:7], -1
	s_waitcnt vmcnt(0)
	v_pk_fma_f32 v[62:63], v[68:69], v[214:215], v[92:93]
	v_pk_fma_f32 v[64:65], v[90:91], v[216:217], v[58:59]
	v_pk_fma_f32 v[58:59], v[66:67], v[228:229], v[94:95]
	v_pk_fma_f32 v[60:61], v[96:97], v[230:231], v[60:61]
	s_cbranch_vccnz .LBB0_1510
	global_store_dwordx4 v[130:131], v[62:65], off offset:-16
	global_store_dwordx4 v[130:131], v[58:61], off
	s_cbranch_execz .LBB0_1511
